# L0 attention idle workgroups convert 13 instead of 9 MoE weight tiles per wave (less left for the router-phase drain)
# speedup vs baseline: 1.0079x; 1.0079x over previous
.LBB0_643:
	s_not_b32 s0, s41
	s_add_i32 s42, s46, s0
	s_mov_b64 s[0:1], -1
	s_cmpk_gt_i32 s42, 0x87
	s_waitcnt vmcnt(0)
	v_lshlrev_b32_e32 v172, 2, v184
	s_cbranch_scc0 .LBB0_720
	s_ashr_i32 s0, s47, 6
	s_lshl_b32 s1, s41, 3
	s_add_i32 s40, s1, s0
	s_add_u32 s41, s6, 0x17458000
	s_mulk_i32 s0, 0x2400
	s_addc_u32 s43, s7, 0
	s_add_i32 s0, s0, 0
	s_add_u32 s44, s6, 0x7458000
	s_addc_u32 s45, s7, 0
	s_add_u32 s47, s6, 0x6458000
	s_addc_u32 s48, s7, 0
	s_add_u32 s49, s6, 0x5458000
	s_addc_u32 s50, s7, 0
	s_add_u32 s51, s6, 0x4d58000
	s_addc_u32 s52, s7, 0
	s_add_u32 s53, s6, 0x158000
	s_addc_u32 s54, s7, 0
	s_add_u32 s55, s6, 0x3390c000
	v_lshlrev_b32_e32 v2, 4, v184
	s_addc_u32 s56, s7, 0
	v_lshlrev_b32_e32 v0, 2, v184
	v_and_b32_e32 v78, 48, v2
	s_add_u32 s57, s6, 0x35e0c000
	v_lshlrev_b32_e32 v2, 1, v184
	v_and_b32_e32 v82, 48, v184
	v_and_b32_e32 v0, 60, v0
	v_bfe_u32 v83, v184, 2, 4
	s_addc_u32 s58, s7, 0
	v_and_b32_e32 v2, 0x60, v2
	v_and_b32_e32 v8, 7, v184
	v_bfe_u32 v87, v184, 3, 3
	v_mov_b32_e32 v77, 0
	v_add_u32_e32 v1, s0, v82
	v_mul_u32_u24_e32 v3, 0x50, v0
	v_add_u32_e32 v4, s0, v78
	v_mul_u32_u24_e32 v5, 0x50, v83
	s_add_u32 s59, s6, 0x3760c000
	v_add_u32_e32 v6, s0, v2
	v_mul_u32_u24_e32 v7, 0x90, v0
	v_lshlrev_b32_e32 v2, 3, v8
	v_lshl_add_u32 v8, v8, 4, s0
	v_mul_u32_u24_e32 v9, 0x90, v87
	s_mul_i32 s40, s40, 13
	s_mov_b32 s1, 0
	v_mov_b32_e32 v79, v77
	v_or_b32_e32 v84, 16, v83
	v_or_b32_e32 v85, 32, v83
	v_or_b32_e32 v86, 48, v83
	s_addc_u32 s60, s7, 0
	v_or_b32_e32 v88, 8, v87
	v_or_b32_e32 v89, 16, v87
	v_or_b32_e32 v90, 24, v87
	v_or_b32_e32 v91, 32, v87
	v_or_b32_e32 v92, 40, v87
	v_or_b32_e32 v93, 48, v87
	v_or_b32_e32 v94, 56, v87
	s_mov_b32 s65, -13
	s_addk_i32 s40, 4
	s_add_i32 s61, 0, 0x204f8
	s_movk_i32 s62, 0x2000
	s_movk_i32 s63, 0x4000
	s_movk_i32 s64, 0x6000
	s_mov_b32 s66, 0x12000
	s_mov_b32 s67, 0xc3e00000
	v_add_u32_e32 v95, v1, v3
	v_add_u32_e32 v96, v4, v5
	s_movk_i32 s68, 0x3000
	s_movk_i32 s69, 0x5000
	s_movk_i32 s70, 0x7000
	s_add_i32 s71, 0, 0x204c0
	s_add_i32 s72, 0, 0x204b8
	s_add_i32 s73, 0, 0x204b0
	s_add_i32 s74, 0, 0x204a8
	s_add_i32 s75, 0, 0x20458
	s_add_i32 s76, 0, 0x20448
	s_add_i32 s77, 0, 0x20440
	s_mov_b32 s78, 0x9000
	s_mov_b32 s79, 0x1b000
	s_mov_b32 s80, 0x25000
	s_mov_b32 s81, 0x2e000
	s_mov_b32 s82, 0x37000
	s_mov_b32 s83, 0x41000
	s_mov_b32 s84, 0x4a000
	s_mov_b32 s85, 0x53000
	s_mov_b32 s86, 0x5d000
	s_mov_b32 s87, 0x66000
	s_mov_b32 s88, 0x6f000
	s_mov_b32 s89, 0x79000
	s_mov_b32 s90, 0x82000
	s_mov_b32 s91, 0x8b000
	v_add_u32_e32 v97, v6, v7
	v_lshlrev_b32_e32 v76, 1, v2
	v_lshlrev_b32_e32 v80, 2, v0
	v_mov_b32_e32 v98, 0x43e00000
	v_mov_b32_e32 v100, v77
	v_mov_b32_e32 v101, v77
	v_mov_b32_e32 v102, v77
	v_mov_b32_e32 v103, v77
	v_add_u32_e32 v99, v8, v9
	s_branch .LBB0_647

.LBB0_1058:
	s_add_i32 s1, s40, 0xffffff78
	s_lshl_b32 s0, s38, 3
	s_max_i32 s1, s1, 0
	s_mulk_i32 s1, 104
	s_add_i32 s0, s42, s0
	s_add_i32 s43, s0, s1
	s_cmpk_gt_i32 s43, 0x5fff
	s_mov_b32 s1, 0
	s_cbranch_scc1 .LBB0_1135
	s_lshl_b32 s44, s40, 3
	s_add_u32 s45, s10, 0x17458000
	s_mul_i32 s0, s42, 0x2400
	s_addc_u32 s46, s11, 0
	s_add_i32 s0, s0, 0
	s_add_u32 s47, s10, 0x7458000
	s_addc_u32 s48, s11, 0
	s_add_u32 s49, s10, 0x6458000
	s_addc_u32 s50, s11, 0
	s_add_u32 s51, s10, 0x5458000
	s_addc_u32 s52, s11, 0
	s_add_u32 s53, s10, 0x4d58000
	s_addc_u32 s54, s11, 0
	s_add_u32 s55, s10, 0x158000
	s_addc_u32 s56, s11, 0
	s_add_u32 s57, s10, 0x3390c000
	s_addc_u32 s58, s11, 0
	s_add_u32 s59, s10, 0x35e0c000
	v_lshlrev_b32_e32 v2, 1, v86
	v_and_b32_e32 v0, 60, v0
	v_and_b32_e32 v80, 48, v54
	s_addc_u32 s60, s11, 0
	v_and_b32_e32 v2, 0x60, v2
	v_and_b32_e32 v8, 7, v85
	v_lshrrev_b32_e32 v90, 3, v86
	v_mov_b32_e32 v79, 0
	v_add_u32_e32 v1, s0, v76
	v_mul_u32_u24_e32 v3, 0x50, v0
	v_add_u32_e32 v4, s0, v80
	v_mul_u32_u24_e32 v5, 0x50, v87
	s_add_u32 s61, s10, 0x3760c000
	v_add_u32_e32 v6, s0, v2
	v_mul_u32_u24_e32 v7, 0x90, v0
	v_lshlrev_b32_e32 v2, 3, v8
	v_lshl_add_u32 v8, v8, 4, s0
	v_mul_u32_u24_e32 v9, 0x90, v90
	v_mov_b32_e32 v81, v79
	v_or_b32_e32 v77, 16, v87
	v_or_b32_e32 v88, 32, v87
	v_or_b32_e32 v89, 48, v87
	s_addc_u32 s62, s11, 0
	v_or_b32_e32 v91, 8, v90
	v_or_b32_e32 v92, 16, v90
	v_or_b32_e32 v93, 24, v90
	v_or_b32_e32 v94, 32, v90
	v_or_b32_e32 v95, 40, v90
	v_or_b32_e32 v96, 48, v90
	v_or_b32_e32 v97, 56, v90
	s_add_i32 s63, 0, 0x204f8
	s_movk_i32 s64, 0x2000
	s_movk_i32 s65, 0x4000
	s_movk_i32 s66, 0x6000
	s_mov_b32 s67, 0x12000
	s_mov_b32 s68, 0xc3e00000
	v_add_u32_e32 v98, v1, v3
	v_add_u32_e32 v99, v4, v5
	s_movk_i32 s69, 0x3000
	s_movk_i32 s70, 0x5000
	s_movk_i32 s71, 0x7000
	s_add_i32 s72, 0, 0x204c0
	s_add_i32 s73, 0, 0x204b8
	s_add_i32 s74, 0, 0x204b0
	s_add_i32 s75, 0, 0x204a8
	s_add_i32 s76, 0, 0x20458
	s_add_i32 s77, 0, 0x20448
	s_add_i32 s78, 0, 0x20440
	s_mov_b32 s79, 0x9000
	s_mov_b32 s80, 0x1b000
	s_mov_b32 s81, 0x25000
	s_mov_b32 s82, 0x2e000
	s_mov_b32 s83, 0x37000
	s_mov_b32 s84, 0x41000
	s_mov_b32 s85, 0x4a000
	s_mov_b32 s86, 0x53000
	s_mov_b32 s87, 0x5d000
	s_mov_b32 s88, 0x66000
	s_mov_b32 s89, 0x6f000
	s_mov_b32 s90, 0x79000
	s_mov_b32 s91, 0x82000
	s_mov_b32 s92, 0x8b000
	v_add_u32_e32 v100, v6, v7
	v_lshlrev_b32_e32 v78, 1, v2
	v_lshlrev_b32_e32 v82, 2, v0
	v_mov_b32_e32 v101, 0x43e00000
	v_mov_b32_e32 v104, v79
	v_mov_b32_e32 v105, v79
	v_mov_b32_e32 v106, v79
	v_mov_b32_e32 v107, v79
	v_add_u32_e32 v102, v8, v9
	s_branch .LBB0_1062
